# P8 tail: peek the conversion queue head with a load before the per-wave atomicAdd (queue is normally exhausted)
# baseline (speedup 1.0000x reference)
; #define LAS __attribute__((address_space(3)))
; #define P0_GET() do { if (DYN) { int v_ = 0x7fffffff; if (lane == 0) { if (!check_stop || __hip_atomic_load(stopw, RLX_AGENT) == 0u) v_ = (int)atomicAdd(qword, 1u); } \
;         idx = __builtin_amdgcn_readfirstlane(v_); ok = idx < P0_NHALF; } else { idx = cur_static; cur_static += nw; ok = idx < s1; } } while (0)
; template <bool DYN>
; __device__ __forceinline__ void p0_walk(const Args& args, unsigned char* ws, LAS float* scr, int lane, int w, int nw, int s0, int s1, unsigned* qword, unsigned* stopw, bool check_stop) {
;     int cur_static = s0 + w, idx = 0; bool ok = false;
;     ...
;     P0_GET();
;     if (!ok) return;
; __global__ void __launch_bounds__(512, 2) mega_fwd(Args args) {
;     ...
;     if (IN(8) && ovl) { p0_walk<true>(args, ws, (LAS float*)(lds + wave * 16384), lane, 0, 0, 0, 0, ctl + CW_CQ, ctl + CW_STOP, false); __syncthreads(); }
.LBB0_2003:
	s_or_b64 exec, exec, s[4:5]
	s_andn2_b64 vcc, exec, s[34:35]
	s_cbranch_vccnz .LBB0_2290
	s_add_u32 s6, s18, 0xc000
	s_addc_u32 s7, s19, 0
	v_mov_b32_e32 v1, 0
	global_load_dword v2, v1, s[6:7] sc1
	s_waitcnt vmcnt(0)
	v_readfirstlane_b32 s3, v2
	s_nop 3
	s_cmpk_gt_u32 s3, 0x5fff
	s_cbranch_scc1 .LBB0_2289
	v_cmp_eq_u32_e64 s[4:5], 0, v164
	v_bfrev_b32_e32 v1, -2
	s_and_saveexec_b64 s[8:9], s[4:5]
	s_cbranch_execz .LBB0_2008
	s_mov_b64 s[12:13], exec
	v_mbcnt_lo_u32_b32 v1, s12, 0
	v_mbcnt_hi_u32_b32 v1, s13, v1
	v_cmp_eq_u32_e32 vcc, 0, v1
	s_and_saveexec_b64 s[10:11], vcc
	s_cbranch_execz .LBB0_2007
	s_bcnt1_i32_b64 s3, s[12:13]
	s_waitcnt vmcnt(15)
	v_mov_b32_e32 v2, 0
	v_mov_b32_e32 v3, s3
	global_atomic_add v2, v2, v3, s[6:7] sc0
